# v76 + wave_sum butterflies of the four rms-norm row loops done with DPP quad/mirror adds and v_permlane16/32_swap instead of six ds_bpermute round trips (bit-identical sums)
# speedup vs baseline: 1.0108x; 1.0001x over previous
.LBB0_2193:
	global_load_dwordx4 v[4:7], v[26:27], off offset:-4096
	global_load_dwordx4 v[0:3], v[26:27], off offset:-4080
	global_load_dwordx4 v[44:47], v[26:27], off offset:-2048
	global_load_dwordx4 v[48:51], v[26:27], off offset:-2032
	global_load_dwordx4 v[52:55], v[26:27], off
	global_load_dwordx4 v[56:59], v[26:27], off offset:16
	global_load_dwordx4 v[208:211], v[26:27], off offset:2048
	global_load_dwordx4 v[212:215], v[26:27], off offset:2064
	v_lshl_add_u64 v[8:9], s[10:11], 0, v[22:23]
	v_lshl_add_u64 v[10:11], s[10:11], 0, v[28:29]
	v_add_co_u32_e32 v64, vcc, s15, v8
	v_add_co_u32_e64 v32, s[2:3], s18, v10
	s_nop 0
	v_addc_co_u32_e32 v65, vcc, 0, v9, vcc
	v_addc_co_u32_e64 v33, s[2:3], 0, v11, s[2:3]
	v_mov_b32_e32 v68, 0
	v_mov_b32_e32 v69, 0
	v_lshl_add_u64 v[30:31], s[10:11], 0, v[24:25]
	s_add_i32 s14, s14, s60
	v_lshl_add_u64 v[24:25], v[24:25], 0, s[4:5]
	v_lshl_add_u64 v[28:29], v[28:29], 0, s[8:9]
	v_lshl_add_u64 v[22:23], v[22:23], 0, s[4:5]
	s_cmpk_lt_i32 s14, 0x4000
	s_waitcnt vmcnt(7)
	v_cvt_pk_bf16_f32 v8, v4, v5
	v_cvt_pk_bf16_f32 v9, v6, v7
	s_waitcnt vmcnt(6)
	v_cvt_pk_bf16_f32 v10, v0, v1
	v_cvt_pk_bf16_f32 v11, v2, v3
	global_store_dwordx4 v[64:65], v[8:11], off
	v_mul_f32_e32 v12, v5, v5
	v_mul_f32_e32 v13, v7, v7
	v_mul_f32_e32 v14, v1, v1
	v_fmac_f32_e32 v12, v4, v4
	v_fmac_f32_e32 v13, v6, v6
	v_mul_f32_e32 v15, v3, v3
	v_fmac_f32_e32 v14, v0, v0
	v_add_f32_e32 v8, v12, v13
	v_fmac_f32_e32 v15, v2, v2
	v_add_f32_e32 v8, v8, v14
	v_add_f32_e32 v12, v15, v8
	s_waitcnt vmcnt(6)
	v_cvt_pk_bf16_f32 v8, v44, v45
	v_cvt_pk_bf16_f32 v9, v46, v47
	s_waitcnt vmcnt(5)
	v_cvt_pk_bf16_f32 v10, v48, v49
	v_cvt_pk_bf16_f32 v11, v50, v51
	global_store_dwordx4 v[64:65], v[8:11], off offset:1024
	v_mul_f32_e32 v13, v45, v45
	v_mul_f32_e32 v14, v47, v47
	v_fmac_f32_e32 v13, v44, v44
	v_mul_f32_e32 v15, v49, v49
	v_fmac_f32_e32 v14, v46, v46
	v_add_f32_e32 v8, v12, v13
	v_mul_f32_e32 v34, v51, v51
	v_fmac_f32_e32 v15, v48, v48
	v_add_f32_e32 v8, v14, v8
	v_fmac_f32_e32 v34, v50, v50
	v_add_f32_e32 v8, v15, v8
	v_add_f32_e32 v34, v34, v8
	s_waitcnt vmcnt(5)
	v_cvt_pk_bf16_f32 v8, v52, v53
	v_cvt_pk_bf16_f32 v9, v54, v55
	s_waitcnt vmcnt(4)
	v_cvt_pk_bf16_f32 v10, v56, v57
	v_cvt_pk_bf16_f32 v11, v58, v59
	global_store_dwordx4 v[64:65], v[8:11], off offset:2048
	v_mul_f32_e32 v43, v53, v53
	v_mul_f32_e32 v60, v55, v55
	v_fmac_f32_e32 v43, v52, v52
	v_mul_f32_e32 v61, v57, v57
	v_fmac_f32_e32 v60, v54, v54
	v_add_f32_e32 v34, v43, v34
	v_mul_f32_e32 v62, v59, v59
	v_fmac_f32_e32 v61, v56, v56
	v_add_f32_e32 v34, v60, v34
	v_fmac_f32_e32 v62, v58, v58
	v_add_f32_e32 v34, v61, v34
	v_add_f32_e32 v34, v62, v34
	v_lshl_add_u64 v[26:27], v[26:27], 0, s[6:7]
	s_waitcnt vmcnt(4)
	v_cvt_pk_bf16_f32 v60, v208, v209
	v_cvt_pk_bf16_f32 v61, v210, v211
	s_waitcnt vmcnt(3)
	v_cvt_pk_bf16_f32 v62, v212, v213
	v_cvt_pk_bf16_f32 v63, v214, v215
	v_pk_mul_f32 v[66:67], v[210:211], v[210:211]
	v_pk_mul_f32 v[70:71], v[208:209], v[208:209]
	global_store_dwordx4 v[64:65], v[60:63], off offset:3072
	v_mov_b32_e32 v76, v66
	v_mov_b32_e32 v77, v70
	v_mov_b32_e32 v70, v67
	v_pk_mul_f32 v[72:73], v[214:215], v[214:215]
	v_pk_mul_f32 v[74:75], v[212:213], v[212:213]
	v_pk_add_f32 v[70:71], v[76:77], v[70:71]
	v_mov_b32_e32 v78, v72
	v_mov_b32_e32 v79, v74
	v_mov_b32_e32 v74, v73
	v_add_f32_e32 v34, v71, v34
	v_pk_add_f32 v[72:73], v[78:79], v[74:75]
	v_add_f32_e32 v34, v70, v34
	v_add_f32_e32 v34, v73, v34
	v_add_f32_e32 v34, v72, v34
	s_nop 1
	v_add_f32_dpp v34, v34, v34 quad_perm:[1,0,3,2] row_mask:0xf bank_mask:0xf
	s_nop 1
	v_add_f32_dpp v34, v34, v34 quad_perm:[2,3,0,1] row_mask:0xf bank_mask:0xf
	s_nop 1
	v_add_f32_dpp v34, v34, v34 row_half_mirror row_mask:0xf bank_mask:0xf
	s_nop 1
	v_add_f32_dpp v34, v34, v34 row_mirror row_mask:0xf bank_mask:0xf
	v_mov_b32_e32 v43, v34
	s_nop 1
	v_permlane16_swap_b32_e32 v34, v43
	v_add_f32_e32 v34, v34, v43
	v_mov_b32_e32 v43, v34
	s_nop 1
	v_permlane32_swap_b32_e32 v34, v43
	v_add_f32_e32 v34, v34, v43
	v_fmamk_f32 v34, v34, 0x3a000000, v41
	v_mul_f32_e32 v43, 0x4b800000, v34
	v_cmp_gt_f32_e32 vcc, s16, v34
	s_nop 1
	v_cndmask_b32_e32 v34, v34, v43, vcc
	v_rsq_f32_e32 v34, v34
	s_nop 0
	v_mul_f32_e32 v43, 0x45800000, v34
	v_cndmask_b32_e32 v34, v34, v43, vcc
	v_pk_mul_f32 v[4:5], v[4:5], v[34:35] op_sel_hi:[1,0]
	v_pk_mul_f32 v[0:1], v[0:1], v[34:35] op_sel_hi:[1,0]
	v_pk_mul_f32 v[6:7], v[6:7], v[34:35] op_sel_hi:[1,0]
	v_pk_mul_f32 v[2:3], v[2:3], v[34:35] op_sel_hi:[1,0]
	v_pk_mul_f32 v[44:45], v[44:45], v[34:35] op_sel_hi:[1,0]
	v_pk_mul_f32 v[48:49], v[48:49], v[34:35] op_sel_hi:[1,0]
	v_pk_mul_f32 v[46:47], v[46:47], v[34:35] op_sel_hi:[1,0]
	v_pk_mul_f32 v[50:51], v[50:51], v[34:35] op_sel_hi:[1,0]
	v_pk_mul_f32 v[208:209], v[208:209], v[34:35] op_sel_hi:[1,0]
	v_pk_mul_f32 v[212:213], v[212:213], v[34:35] op_sel_hi:[1,0]
	v_pk_mul_f32 v[210:211], v[210:211], v[34:35] op_sel_hi:[1,0]
	v_pk_mul_f32 v[214:215], v[214:215], v[34:35] op_sel_hi:[1,0]
	v_pk_mul_f32 v[4:5], v[176:177], v[4:5]
	v_pk_mul_f32 v[60:61], v[180:181], v[0:1]
	v_pk_mul_f32 v[6:7], v[178:179], v[6:7]
	v_pk_mul_f32 v[62:63], v[182:183], v[2:3]
	v_mul_f32_e32 v43, 0x42000000, v4
	v_mul_f32_e32 v64, 0x42000000, v5
	v_mul_f32_e32 v67, 0x42000000, v60
	v_mul_f32_e32 v70, 0x42000000, v61
	v_cvt_pk_bf16_f32 v0, v4, v5
	v_cvt_pk_bf16_f32 v2, v60, v61
	v_med3_f32 v4, v43, s17, v42
	v_med3_f32 v5, v64, s17, v42
	v_med3_f32 v43, v67, s17, v42
	v_med3_f32 v60, v70, s17, v42
	v_cvt_pk_fp8_f32 v68, v4, v5
	v_cvt_pk_fp8_f32 v69, v43, v60
	v_mul_f32_e32 v65, 0x42000000, v6
	v_mul_f32_e32 v66, 0x42000000, v7
	v_mul_f32_e32 v71, 0x42000000, v62
	v_mul_f32_e32 v72, 0x42000000, v63
	v_cvt_pk_bf16_f32 v1, v6, v7
	v_cvt_pk_bf16_f32 v3, v62, v63
	v_med3_f32 v6, v65, s17, v42
	v_med3_f32 v7, v66, s17, v42
	v_med3_f32 v61, v71, s17, v42
	v_med3_f32 v62, v72, s17, v42
	v_cvt_pk_fp8_f32 v68, v6, v7 op_sel:[0,0,1]
	v_cvt_pk_fp8_f32 v69, v61, v62 op_sel:[0,0,1]
	global_store_dwordx2 v[32:33], v[68:69], off
	global_store_dwordx4 v[30:31], v[0:3], off
	v_mov_b32_e32 v60, 0
	v_mov_b32_e32 v61, 0
	v_pk_mul_f32 v[0:1], v[184:185], v[44:45]
	v_pk_mul_f32 v[4:5], v[188:189], v[48:49]
	v_pk_mul_f32 v[2:3], v[186:187], v[46:47]
	v_mul_f32_e32 v43, 0x42000000, v0
	v_mul_f32_e32 v44, 0x42000000, v1
	v_mul_f32_e32 v47, 0x42000000, v4
	v_mul_f32_e32 v48, 0x42000000, v5
	v_mul_f32_e32 v45, 0x42000000, v2
	v_cvt_pk_bf16_f32 v0, v0, v1
	v_cvt_pk_bf16_f32 v1, v2, v3
	v_cvt_pk_bf16_f32 v2, v4, v5
	v_med3_f32 v4, v43, s17, v42
	v_med3_f32 v5, v44, s17, v42
	v_med3_f32 v43, v47, s17, v42
	v_med3_f32 v44, v48, s17, v42
	v_cvt_pk_fp8_f32 v60, v4, v5
	v_cvt_pk_fp8_f32 v61, v43, v44
	v_pk_mul_f32 v[6:7], v[190:191], v[50:51]
	v_mul_f32_e32 v46, 0x42000000, v3
	v_mul_f32_e32 v49, 0x42000000, v6
	v_mul_f32_e32 v50, 0x42000000, v7
	v_cvt_pk_bf16_f32 v3, v6, v7
	v_med3_f32 v6, v45, s17, v42
	v_med3_f32 v7, v46, s17, v42
	v_med3_f32 v45, v49, s17, v42
	v_med3_f32 v46, v50, s17, v42
	v_cvt_pk_fp8_f32 v60, v6, v7 op_sel:[0,0,1]
	v_cvt_pk_fp8_f32 v61, v45, v46 op_sel:[0,0,1]
	global_store_dwordx2 v[32:33], v[60:61], off offset:512
	global_store_dwordx4 v[30:31], v[0:3], off offset:1024
	v_pk_mul_f32 v[46:47], v[52:53], v[34:35] op_sel_hi:[1,0]
	v_pk_mul_f32 v[48:49], v[56:57], v[34:35] op_sel_hi:[1,0]
	v_pk_mul_f32 v[50:51], v[54:55], v[34:35] op_sel_hi:[1,0]
	v_mov_b32_e32 v44, 0
	v_mov_b32_e32 v45, 0
	v_pk_mul_f32 v[52:53], v[58:59], v[34:35] op_sel_hi:[1,0]
	v_pk_mul_f32 v[0:1], v[46:47], v[192:193]
	v_pk_mul_f32 v[4:5], v[48:49], v[196:197]
	v_pk_mul_f32 v[2:3], v[50:51], v[194:195]
	v_mul_f32_e32 v43, 0x42000000, v0
	v_mul_f32_e32 v46, 0x42000000, v1
	v_mul_f32_e32 v49, 0x42000000, v4
	v_mul_f32_e32 v50, 0x42000000, v5
	v_mul_f32_e32 v47, 0x42000000, v2
	v_cvt_pk_bf16_f32 v0, v0, v1
	v_cvt_pk_bf16_f32 v1, v2, v3
	v_cvt_pk_bf16_f32 v2, v4, v5
	v_med3_f32 v4, v43, s17, v42
	v_med3_f32 v5, v46, s17, v42
	v_med3_f32 v43, v49, s17, v42
	v_med3_f32 v46, v50, s17, v42
	v_cvt_pk_fp8_f32 v44, v4, v5
	v_cvt_pk_fp8_f32 v45, v43, v46
	v_pk_mul_f32 v[6:7], v[52:53], v[198:199]
	v_mul_f32_e32 v48, 0x42000000, v3
	v_mul_f32_e32 v51, 0x42000000, v6
	v_mul_f32_e32 v52, 0x42000000, v7
	v_cvt_pk_bf16_f32 v3, v6, v7
	v_med3_f32 v6, v47, s17, v42
	v_med3_f32 v7, v48, s17, v42
	v_med3_f32 v47, v51, s17, v42
	v_med3_f32 v48, v52, s17, v42
	v_cvt_pk_fp8_f32 v44, v6, v7 op_sel:[0,0,1]
	v_cvt_pk_fp8_f32 v45, v47, v48 op_sel:[0,0,1]
	global_store_dwordx2 v[32:33], v[44:45], off offset:1024
	global_store_dwordx4 v[30:31], v[0:3], off offset:2048
	v_mov_b32_e32 v44, 0
	v_mov_b32_e32 v45, 0
	v_pk_mul_f32 v[0:1], v[208:209], v[200:201]
	v_pk_mul_f32 v[4:5], v[212:213], v[204:205]
	v_pk_mul_f32 v[2:3], v[210:211], v[202:203]
	v_pk_mul_f32 v[6:7], v[214:215], v[206:207]
	v_mul_f32_e32 v8, 0x42000000, v0
	v_mul_f32_e32 v9, 0x42000000, v1
	v_mul_f32_e32 v10, 0x42000000, v2
	v_mul_f32_e32 v11, 0x42000000, v3
	v_mul_f32_e32 v12, 0x42000000, v4
	v_mul_f32_e32 v13, 0x42000000, v5
	v_cvt_pk_bf16_f32 v0, v0, v1
	v_cvt_pk_bf16_f32 v1, v2, v3
	v_med3_f32 v2, v8, s17, v42
	v_med3_f32 v3, v9, s17, v42
	v_med3_f32 v8, v10, s17, v42
	v_med3_f32 v9, v11, s17, v42
	v_med3_f32 v10, v12, s17, v42
	v_med3_f32 v11, v13, s17, v42
	v_cvt_pk_fp8_f32 v44, v2, v3
	v_cvt_pk_fp8_f32 v45, v10, v11
	v_mul_f32_e32 v14, 0x42000000, v6
	v_mul_f32_e32 v15, 0x42000000, v7
	v_med3_f32 v12, v14, s17, v42
	v_med3_f32 v2, v15, s17, v42
	v_cvt_pk_fp8_f32 v44, v8, v9 op_sel:[0,0,1]
	v_cvt_pk_fp8_f32 v45, v12, v2 op_sel:[0,0,1]
	v_cvt_pk_bf16_f32 v2, v4, v5
	v_cvt_pk_bf16_f32 v3, v6, v7
	global_store_dwordx2 v[32:33], v[44:45], off offset:1536
	global_store_dwordx4 v[30:31], v[0:3], off offset:3072
	s_cbranch_scc1 .LBB0_2193

.LBB0_2271:
	v_lshl_add_u64 v[20:21], s[12:13], 0, v[16:17]
	s_mov_b32 s15, 0x15e00000
	v_add_co_u32_e32 v32, vcc, s15, v20
	v_lshl_add_u64 v[24:25], s[12:13], 0, v[14:15]
	v_addc_co_u32_e32 v33, vcc, 0, v21, vcc
	v_add_co_u32_e32 v20, vcc, s21, v24
	s_nop 0
	v_addc_co_u32_e32 v21, vcc, 0, v25, vcc
	s_add_u32 s6, s12, s0
	s_addc_u32 s7, s13, s3
	s_add_i32 s15, 0, 0x20200
	v_mov_b32_e32 v22, v1
	v_mov_b32_e32 v23, v1
	v_lshl_add_u64 v[18:19], s[12:13], 0, v[12:13]
	s_add_i32 s14, s14, s22
	v_lshl_add_u64 v[12:13], v[12:13], 0, s[74:75]
	v_lshl_add_u64 v[14:15], v[14:15], 0, s[66:67]
	v_lshl_add_u64 v[16:17], v[16:17], 0, s[74:75]
	v_readfirstlane_b32 s16, v246
	v_readfirstlane_b32 s18, v248
	s_lshl_b32 s16, s16, 2
	s_lshl_b32 s18, s18, 2
	s_add_i32 s16, s15, s16
	s_add_i32 s15, s15, s18
	v_mov_b32_e32 v0, s16
	v_mov_b32_e32 v24, s15
	ds_read_b32 v0, v0
	ds_read_b32 v41, v24
	v_readfirstlane_b32 s17, v247
	v_readfirstlane_b32 s19, v249
	s_add_u32 s98, s4, s80
	s_addc_u32 s99, s5, s81
	s_add_u32 s98, s98, s12
	s_addc_u32 s99, s99, s13
	global_load_dwordx4 v[246:249], v250, s[98:99]
	global_load_dwordx4 v[24:27], v[32:33], off
	global_load_dwordx4 v[28:31], v[32:33], off offset:1024
	global_load_dwordx4 v[42:45], v[32:33], off offset:2048
	global_load_dwordx2 v[58:59], v1, s[6:7]
	global_load_dwordx4 v[46:49], v[32:33], off offset:3072
	s_waitcnt lgkmcnt(1)
	v_readfirstlane_b32 s6, v0
	s_waitcnt lgkmcnt(0)
	v_readfirstlane_b32 s7, v41
	s_lshl_b32 s7, s7, 8
	s_lshl_b32 s6, s6, 8
	s_add_i32 s16, s7, s19
	s_add_i32 s6, s6, s17
	s_ashr_i32 s17, s16, 31
	s_ashr_i32 s7, s6, 31
	s_lshl_b64 s[16:17], s[16:17], 12
	s_lshl_b64 s[6:7], s[6:7], 12
	v_lshl_add_u64 v[62:63], v[10:11], 0, s[16:17]
	v_lshl_add_u64 v[60:61], v[10:11], 0, s[6:7]
	global_load_dwordx4 v[50:53], v[62:63], off
	global_load_dwordx4 v[54:57], v[60:61], off
	global_load_dwordx4 v[198:201], v[62:63], off offset:1024
	global_load_dwordx4 v[202:205], v[60:61], off offset:1024
	global_load_dwordx4 v[206:209], v[62:63], off offset:2048
	global_load_dwordx4 v[210:213], v[60:61], off offset:2048
	global_load_dwordx4 v[214:217], v[62:63], off offset:3072
	global_load_dwordx4 v[242:245], v[60:61], off offset:3072
	s_add_u32 s4, s4, s80
	s_addc_u32 s5, s5, s81
	s_add_u32 s0, s0, s84
	s_addc_u32 s3, s3, s85
	s_cmpk_gt_i32 s14, 0x3fff
	s_waitcnt vmcnt(12)
	v_lshlrev_b32_e32 v64, 16, v27
	v_and_b32_e32 v65, 0xffff0000, v27
	v_lshlrev_b32_e32 v68, 16, v26
	v_and_b32_e32 v69, 0xffff0000, v26
	s_waitcnt vmcnt(11)
	v_lshlrev_b32_e32 v70, 16, v28
	v_and_b32_e32 v71, 0xffff0000, v28
	v_lshlrev_b32_e32 v72, 16, v29
	v_and_b32_e32 v73, 0xffff0000, v29
	v_lshlrev_b32_e32 v74, 16, v30
	v_and_b32_e32 v75, 0xffff0000, v30
	v_lshlrev_b32_e32 v76, 16, v31
	v_and_b32_e32 v77, 0xffff0000, v31
	v_lshlrev_b32_e32 v66, 16, v24
	v_and_b32_e32 v67, 0xffff0000, v24
	v_lshlrev_b32_e32 v24, 16, v25
	v_and_b32_e32 v25, 0xffff0000, v25
	s_waitcnt vmcnt(7)
	v_lshlrev_b32_e32 v26, 16, v50
	s_waitcnt vmcnt(6)
	v_and_b32_e32 v27, 0xffff0000, v54
	v_lshlrev_b32_e32 v28, 16, v54
	v_and_b32_e32 v29, 0xffff0000, v50
	v_lshlrev_b32_e32 v30, 16, v51
	v_lshlrev_b32_e32 v50, 16, v55
	v_and_b32_e32 v51, 0xffff0000, v51
	v_lshlrev_b32_e32 v54, 16, v52
	v_lshlrev_b32_e32 v86, 16, v56
	v_and_b32_e32 v87, 0xffff0000, v52
	v_lshlrev_b32_e32 v88, 16, v53
	v_lshlrev_b32_e32 v52, 16, v57
	v_and_b32_e32 v53, 0xffff0000, v53
	v_and_b32_e32 v31, 0xffff0000, v55
	v_and_b32_e32 v55, 0xffff0000, v56
	v_and_b32_e32 v89, 0xffff0000, v57
	v_pk_mul_f32 v[28:29], v[58:59], v[28:29]
	v_pk_mul_f32 v[50:51], v[58:59], v[50:51]
	v_pk_mul_f32 v[56:57], v[58:59], v[86:87]
	v_pk_mul_f32 v[52:53], v[58:59], v[52:53]
	v_pk_fma_f32 v[26:27], v[58:59], v[26:27], v[28:29] op_sel:[1,0,0] op_sel_hi:[0,1,1]
	v_pk_fma_f32 v[28:29], v[58:59], v[30:31], v[50:51] op_sel:[1,0,0] op_sel_hi:[0,1,1]
	v_pk_fma_f32 v[30:31], v[58:59], v[54:55], v[56:57] op_sel:[1,0,0] op_sel_hi:[0,1,1]
	v_pk_fma_f32 v[50:51], v[58:59], v[88:89], v[52:53] op_sel:[1,0,0] op_sel_hi:[0,1,1]
	v_pk_add_f32 v[52:53], v[26:27], v[66:67]
	v_pk_add_f32 v[54:55], v[28:29], v[24:25]
	v_pk_add_f32 v[56:57], v[30:31], v[68:69]
	v_pk_add_f32 v[50:51], v[50:51], v[64:65]
	v_cvt_pk_bf16_f32 v24, v52, v53
	v_cvt_pk_bf16_f32 v25, v54, v55
	v_cvt_pk_bf16_f32 v26, v56, v57
	v_cvt_pk_bf16_f32 v27, v50, v51
	v_pk_mul_f32 v[28:29], v[52:53], v[52:53]
	v_pk_mul_f32 v[30:31], v[54:55], v[54:55]
	v_pk_mul_f32 v[66:67], v[50:51], v[50:51]
	global_store_dwordx4 v[32:33], v[24:27], off
	v_add_f32_e32 v0, v66, v67
	v_add_f32_e32 v41, v30, v31
	v_add_f32_e32 v66, v28, v29
	v_pk_mul_f32 v[64:65], v[56:57], v[56:57]
	v_add_f32_e32 v41, v66, v41
	v_add_f32_e32 v64, v64, v65
	v_add_f32_e32 v41, v64, v41
	v_add_f32_e32 v0, v0, v41
	v_lshlrev_b32_e32 v78, 16, v42
	v_and_b32_e32 v79, 0xffff0000, v42
	v_lshlrev_b32_e32 v42, 16, v43
	v_and_b32_e32 v43, 0xffff0000, v43
	v_lshlrev_b32_e32 v80, 16, v44
	v_and_b32_e32 v81, 0xffff0000, v44
	v_lshlrev_b32_e32 v44, 16, v45
	v_and_b32_e32 v45, 0xffff0000, v45
	v_lshlrev_b32_e32 v82, 16, v46
	v_and_b32_e32 v83, 0xffff0000, v46
	v_lshlrev_b32_e32 v46, 16, v47
	v_and_b32_e32 v47, 0xffff0000, v47
	v_lshlrev_b32_e32 v84, 16, v48
	v_and_b32_e32 v85, 0xffff0000, v48
	v_lshlrev_b32_e32 v48, 16, v49
	v_and_b32_e32 v49, 0xffff0000, v49
	s_waitcnt vmcnt(5)
	v_lshlrev_b32_e32 v64, 16, v198
	s_waitcnt vmcnt(4)
	v_and_b32_e32 v65, 0xffff0000, v202
	v_lshlrev_b32_e32 v66, 16, v202
	v_and_b32_e32 v67, 0xffff0000, v198
	v_lshlrev_b32_e32 v68, 16, v199
	v_lshlrev_b32_e32 v24, 16, v203
	v_and_b32_e32 v25, 0xffff0000, v199
	v_lshlrev_b32_e32 v28, 16, v200
	v_lshlrev_b32_e32 v86, 16, v204
	v_and_b32_e32 v87, 0xffff0000, v200
	v_lshlrev_b32_e32 v88, 16, v201
	v_lshlrev_b32_e32 v26, 16, v205
	v_and_b32_e32 v27, 0xffff0000, v201
	v_and_b32_e32 v69, 0xffff0000, v203
	v_and_b32_e32 v29, 0xffff0000, v204
	v_and_b32_e32 v89, 0xffff0000, v205
	v_pk_mul_f32 v[30:31], v[58:59], v[66:67]
	v_pk_mul_f32 v[24:25], v[58:59], v[24:25]
	v_pk_mul_f32 v[66:67], v[58:59], v[86:87]
	v_pk_mul_f32 v[26:27], v[58:59], v[26:27]
	v_pk_fma_f32 v[30:31], v[58:59], v[64:65], v[30:31] op_sel:[1,0,0] op_sel_hi:[0,1,1]
	v_pk_fma_f32 v[24:25], v[58:59], v[68:69], v[24:25] op_sel:[1,0,0] op_sel_hi:[0,1,1]
	v_pk_fma_f32 v[28:29], v[58:59], v[28:29], v[66:67] op_sel:[1,0,0] op_sel_hi:[0,1,1]
	v_pk_fma_f32 v[26:27], v[58:59], v[88:89], v[26:27] op_sel:[1,0,0] op_sel_hi:[0,1,1]
	v_pk_add_f32 v[64:65], v[30:31], v[70:71]
	v_pk_add_f32 v[66:67], v[24:25], v[72:73]
	v_pk_add_f32 v[68:69], v[28:29], v[74:75]
	v_pk_add_f32 v[70:71], v[26:27], v[76:77]
	v_cvt_pk_bf16_f32 v24, v64, v65
	v_cvt_pk_bf16_f32 v25, v66, v67
	v_cvt_pk_bf16_f32 v26, v68, v69
	v_cvt_pk_bf16_f32 v27, v70, v71
	v_pk_mul_f32 v[28:29], v[64:65], v[64:65]
	v_pk_mul_f32 v[30:31], v[66:67], v[66:67]
	global_store_dwordx4 v[32:33], v[24:27], off offset:1024
	v_add_f32_e32 v41, v28, v29
	v_add_f32_e32 v76, v30, v31
	v_pk_mul_f32 v[72:73], v[68:69], v[68:69]
	v_add_f32_e32 v0, v0, v41
	v_pk_mul_f32 v[74:75], v[70:71], v[70:71]
	v_add_f32_e32 v72, v72, v73
	v_add_f32_e32 v0, v76, v0
	v_add_f32_e32 v73, v74, v75
	v_add_f32_e32 v0, v72, v0
	v_add_f32_e32 v0, v73, v0
	s_waitcnt vmcnt(3)
	v_lshlrev_b32_e32 v72, 16, v206
	s_waitcnt vmcnt(2)
	v_and_b32_e32 v73, 0xffff0000, v210
	v_lshlrev_b32_e32 v74, 16, v210
	v_and_b32_e32 v75, 0xffff0000, v206
	v_lshlrev_b32_e32 v76, 16, v207
	v_lshlrev_b32_e32 v24, 16, v211
	v_and_b32_e32 v25, 0xffff0000, v207
	v_lshlrev_b32_e32 v28, 16, v208
	v_lshlrev_b32_e32 v86, 16, v212
	v_and_b32_e32 v87, 0xffff0000, v208
	v_lshlrev_b32_e32 v88, 16, v209
	v_lshlrev_b32_e32 v26, 16, v213
	v_and_b32_e32 v27, 0xffff0000, v209
	v_and_b32_e32 v77, 0xffff0000, v211
	v_and_b32_e32 v29, 0xffff0000, v212
	v_and_b32_e32 v89, 0xffff0000, v213
	v_pk_mul_f32 v[30:31], v[58:59], v[74:75]
	v_pk_mul_f32 v[24:25], v[58:59], v[24:25]
	v_pk_mul_f32 v[74:75], v[58:59], v[86:87]
	v_pk_mul_f32 v[26:27], v[58:59], v[26:27]
	v_pk_fma_f32 v[30:31], v[58:59], v[72:73], v[30:31] op_sel:[1,0,0] op_sel_hi:[0,1,1]
	v_pk_fma_f32 v[24:25], v[58:59], v[76:77], v[24:25] op_sel:[1,0,0] op_sel_hi:[0,1,1]
	v_pk_fma_f32 v[28:29], v[58:59], v[28:29], v[74:75] op_sel:[1,0,0] op_sel_hi:[0,1,1]
	v_pk_fma_f32 v[26:27], v[58:59], v[88:89], v[26:27] op_sel:[1,0,0] op_sel_hi:[0,1,1]
	v_pk_add_f32 v[72:73], v[30:31], v[78:79]
	v_pk_add_f32 v[74:75], v[24:25], v[42:43]
	v_pk_add_f32 v[76:77], v[28:29], v[80:81]
	v_pk_add_f32 v[78:79], v[26:27], v[44:45]
	v_cvt_pk_bf16_f32 v24, v72, v73
	v_cvt_pk_bf16_f32 v25, v74, v75
	v_cvt_pk_bf16_f32 v26, v76, v77
	v_cvt_pk_bf16_f32 v27, v78, v79
	v_pk_mul_f32 v[28:29], v[72:73], v[72:73]
	v_pk_mul_f32 v[30:31], v[74:75], v[74:75]
	global_store_dwordx4 v[32:33], v[24:27], off offset:2048
	v_add_f32_e32 v41, v28, v29
	v_add_f32_e32 v80, v30, v31
	v_pk_mul_f32 v[42:43], v[76:77], v[76:77]
	v_add_f32_e32 v0, v0, v41
	v_pk_mul_f32 v[44:45], v[78:79], v[78:79]
	v_add_f32_e32 v42, v42, v43
	v_add_f32_e32 v0, v80, v0
	v_add_f32_e32 v43, v44, v45
	v_add_f32_e32 v0, v42, v0
	v_add_f32_e32 v0, v43, v0
	s_waitcnt vmcnt(1)
	v_lshlrev_b32_e32 v42, 16, v214
	s_waitcnt vmcnt(0)
	v_and_b32_e32 v43, 0xffff0000, v242
	v_lshlrev_b32_e32 v44, 16, v242
	v_and_b32_e32 v45, 0xffff0000, v214
	v_lshlrev_b32_e32 v60, 16, v215
	v_lshlrev_b32_e32 v24, 16, v243
	v_and_b32_e32 v25, 0xffff0000, v215
	v_lshlrev_b32_e32 v28, 16, v216
	v_lshlrev_b32_e32 v62, 16, v244
	v_and_b32_e32 v63, 0xffff0000, v216
	v_lshlrev_b32_e32 v80, 16, v217
	v_lshlrev_b32_e32 v26, 16, v245
	v_and_b32_e32 v27, 0xffff0000, v217
	v_and_b32_e32 v61, 0xffff0000, v243
	v_and_b32_e32 v29, 0xffff0000, v244
	v_and_b32_e32 v81, 0xffff0000, v245
	v_pk_mul_f32 v[30:31], v[58:59], v[44:45]
	v_pk_mul_f32 v[24:25], v[58:59], v[24:25]
	v_pk_mul_f32 v[44:45], v[58:59], v[62:63]
	v_pk_mul_f32 v[26:27], v[58:59], v[26:27]
	v_pk_fma_f32 v[30:31], v[58:59], v[42:43], v[30:31] op_sel:[1,0,0] op_sel_hi:[0,1,1]
	v_pk_fma_f32 v[24:25], v[58:59], v[60:61], v[24:25] op_sel:[1,0,0] op_sel_hi:[0,1,1]
	v_pk_fma_f32 v[28:29], v[58:59], v[28:29], v[44:45] op_sel:[1,0,0] op_sel_hi:[0,1,1]
	v_pk_fma_f32 v[42:43], v[58:59], v[80:81], v[26:27] op_sel:[1,0,0] op_sel_hi:[0,1,1]
	v_pk_add_f32 v[26:27], v[30:31], v[82:83]
	v_pk_add_f32 v[24:25], v[24:25], v[46:47]
	v_pk_add_f32 v[30:31], v[28:29], v[84:85]
	v_pk_add_f32 v[28:29], v[42:43], v[48:49]
	v_cvt_pk_bf16_f32 v42, v26, v27
	v_cvt_pk_bf16_f32 v43, v24, v25
	v_cvt_pk_bf16_f32 v44, v30, v31
	v_cvt_pk_bf16_f32 v45, v28, v29
	v_mov_b32_e32 v46, v25
	v_mov_b32_e32 v47, v27
	v_mov_b32_e32 v48, v29
	v_mov_b32_e32 v49, v31
	global_store_dwordx4 v[32:33], v[42:45], off offset:3072
	v_pk_mul_f32 v[32:33], v[46:47], v[46:47]
	v_pk_mul_f32 v[62:63], v[48:49], v[48:49]
	v_mov_b32_e32 v58, v24
	v_mov_b32_e32 v59, v26
	v_pk_fma_f32 v[32:33], v[58:59], v[58:59], v[32:33]
	v_mov_b32_e32 v60, v28
	v_mov_b32_e32 v61, v30
	v_add_f32_e32 v0, v0, v33
	v_pk_fma_f32 v[58:59], v[60:61], v[60:61], v[62:63]
	v_add_f32_e32 v0, v32, v0
	v_add_f32_e32 v0, v59, v0
	v_add_f32_e32 v0, v58, v0
	s_nop 1
	v_add_f32_dpp v0, v0, v0 quad_perm:[1,0,3,2] row_mask:0xf bank_mask:0xf
	s_nop 1
	v_add_f32_dpp v0, v0, v0 quad_perm:[2,3,0,1] row_mask:0xf bank_mask:0xf
	s_nop 1
	v_add_f32_dpp v0, v0, v0 row_half_mirror row_mask:0xf bank_mask:0xf
	s_nop 1
	v_add_f32_dpp v0, v0, v0 row_mirror row_mask:0xf bank_mask:0xf
	v_mov_b32_e32 v32, v0
	s_nop 1
	v_permlane16_swap_b32_e32 v0, v32
	v_add_f32_e32 v0, v0, v32
	v_mov_b32_e32 v32, v0
	s_nop 1
	v_permlane32_swap_b32_e32 v0, v32
	v_add_f32_e32 v0, v0, v32
	v_fmamk_f32 v0, v0, 0x3a000000, v220
	v_mul_f32_e32 v32, 0x4b800000, v0
	v_cmp_gt_f32_e32 vcc, s65, v0
	s_nop 1
	v_cndmask_b32_e32 v0, v0, v32, vcc
	v_rsq_f32_e32 v0, v0
	s_nop 0
	v_mul_f32_e32 v32, 0x45800000, v0
	v_cndmask_b32_e32 v0, v0, v32, vcc
	v_pk_mul_f32 v[32:33], v[52:53], v[0:1] op_sel_hi:[1,0]
	v_pk_mul_f32 v[52:53], v[56:57], v[0:1] op_sel_hi:[1,0]
	v_pk_mul_f32 v[54:55], v[54:55], v[0:1] op_sel_hi:[1,0]
	v_pk_mul_f32 v[50:51], v[50:51], v[0:1] op_sel_hi:[1,0]
	v_pk_mul_f32 v[24:25], v[24:25], v[0:1] op_sel_hi:[1,0]
	v_pk_mul_f32 v[28:29], v[28:29], v[0:1] op_sel_hi:[1,0]
	v_pk_mul_f32 v[32:33], v[156:157], v[32:33]
	v_pk_mul_f32 v[46:47], v[160:161], v[52:53]
	v_pk_mul_f32 v[44:45], v[158:159], v[54:55]
	v_pk_mul_f32 v[48:49], v[162:163], v[50:51]
	v_mul_f32_e32 v41, 0x42000000, v32
	v_mul_f32_e32 v50, 0x42000000, v33
	v_mul_f32_e32 v53, 0x42000000, v46
	v_mul_f32_e32 v54, 0x42000000, v47
	v_mul_f32_e32 v51, 0x42000000, v44
	v_mul_f32_e32 v52, 0x42000000, v45
	v_mul_f32_e32 v55, 0x42000000, v48
	v_cvt_pk_bf16_f32 v42, v32, v33
	v_cvt_pk_bf16_f32 v43, v44, v45
	v_cvt_pk_bf16_f32 v44, v46, v47
	v_cvt_pk_bf16_f32 v45, v48, v49
	v_med3_f32 v32, v41, s76, v237
	v_med3_f32 v33, v50, s76, v237
	v_med3_f32 v47, v53, s76, v237
	v_med3_f32 v48, v54, s76, v237
	v_cvt_pk_fp8_f32 v22, v32, v33
	v_cvt_pk_fp8_f32 v23, v47, v48
	v_mul_f32_e32 v56, 0x42000000, v49
	v_med3_f32 v41, v51, s76, v237
	v_med3_f32 v46, v52, s76, v237
	v_med3_f32 v49, v55, s76, v237
	v_med3_f32 v50, v56, s76, v237
	v_cvt_pk_fp8_f32 v22, v41, v46 op_sel:[0,0,1]
	v_cvt_pk_fp8_f32 v23, v49, v50 op_sel:[0,0,1]
	global_store_dwordx2 v[20:21], v[22:23], off
	global_store_dwordx4 v[18:19], v[42:45], off
	v_pk_mul_f32 v[32:33], v[64:65], v[0:1] op_sel_hi:[1,0]
	v_pk_mul_f32 v[50:51], v[68:69], v[0:1] op_sel_hi:[1,0]
	v_pk_mul_f32 v[52:53], v[66:67], v[0:1] op_sel_hi:[1,0]
	v_pk_mul_f32 v[54:55], v[70:71], v[0:1] op_sel_hi:[1,0]
	v_mov_b32_e32 v22, v1
	v_mov_b32_e32 v23, v1
	v_pk_mul_f32 v[32:33], v[164:165], v[32:33]
	v_pk_mul_f32 v[46:47], v[168:169], v[50:51]
	v_pk_mul_f32 v[44:45], v[166:167], v[52:53]
	v_pk_mul_f32 v[48:49], v[170:171], v[54:55]
	v_mul_f32_e32 v41, 0x42000000, v32
	v_mul_f32_e32 v50, 0x42000000, v33
	v_mul_f32_e32 v53, 0x42000000, v46
	v_mul_f32_e32 v54, 0x42000000, v47
	v_mul_f32_e32 v51, 0x42000000, v44
	v_mul_f32_e32 v52, 0x42000000, v45
	v_mul_f32_e32 v55, 0x42000000, v48
	v_cvt_pk_bf16_f32 v42, v32, v33
	v_cvt_pk_bf16_f32 v43, v44, v45
	v_cvt_pk_bf16_f32 v44, v46, v47
	v_cvt_pk_bf16_f32 v45, v48, v49
	v_med3_f32 v32, v41, s76, v237
	v_med3_f32 v33, v50, s76, v237
	v_med3_f32 v47, v53, s76, v237
	v_med3_f32 v48, v54, s76, v237
	v_cvt_pk_fp8_f32 v22, v32, v33
	v_cvt_pk_fp8_f32 v23, v47, v48
	v_mul_f32_e32 v56, 0x42000000, v49
	v_med3_f32 v41, v51, s76, v237
	v_med3_f32 v46, v52, s76, v237
	v_med3_f32 v49, v55, s76, v237
	v_med3_f32 v50, v56, s76, v237
	v_cvt_pk_fp8_f32 v22, v41, v46 op_sel:[0,0,1]
	v_cvt_pk_fp8_f32 v23, v49, v50 op_sel:[0,0,1]
	global_store_dwordx2 v[20:21], v[22:23], off offset:512
	global_store_dwordx4 v[18:19], v[42:45], off offset:1024
	v_pk_mul_f32 v[32:33], v[72:73], v[0:1] op_sel_hi:[1,0]
	v_pk_mul_f32 v[50:51], v[76:77], v[0:1] op_sel_hi:[1,0]
	v_pk_mul_f32 v[52:53], v[74:75], v[0:1] op_sel_hi:[1,0]
	v_pk_mul_f32 v[54:55], v[78:79], v[0:1] op_sel_hi:[1,0]
	v_mov_b32_e32 v22, v1
	v_mov_b32_e32 v23, v1
	v_pk_mul_f32 v[32:33], v[172:173], v[32:33]
	v_pk_mul_f32 v[46:47], v[176:177], v[50:51]
	v_pk_mul_f32 v[44:45], v[174:175], v[52:53]
	v_pk_mul_f32 v[48:49], v[178:179], v[54:55]
	v_mul_f32_e32 v41, 0x42000000, v32
	v_mul_f32_e32 v50, 0x42000000, v33
	v_mul_f32_e32 v53, 0x42000000, v46
	v_mul_f32_e32 v54, 0x42000000, v47
	v_mul_f32_e32 v51, 0x42000000, v44
	v_mul_f32_e32 v52, 0x42000000, v45
	v_mul_f32_e32 v55, 0x42000000, v48
	v_cvt_pk_bf16_f32 v42, v32, v33
	v_cvt_pk_bf16_f32 v43, v44, v45
	v_cvt_pk_bf16_f32 v44, v46, v47
	v_cvt_pk_bf16_f32 v45, v48, v49
	v_med3_f32 v32, v41, s76, v237
	v_med3_f32 v33, v50, s76, v237
	v_med3_f32 v47, v53, s76, v237
	v_med3_f32 v48, v54, s76, v237
	v_cvt_pk_fp8_f32 v22, v32, v33
	v_cvt_pk_fp8_f32 v23, v47, v48
	v_mul_f32_e32 v56, 0x42000000, v49
	v_med3_f32 v41, v51, s76, v237
	v_med3_f32 v46, v52, s76, v237
	v_med3_f32 v49, v55, s76, v237
	v_med3_f32 v50, v56, s76, v237
	v_cvt_pk_fp8_f32 v22, v41, v46 op_sel:[0,0,1]
	v_cvt_pk_fp8_f32 v23, v49, v50 op_sel:[0,0,1]
	global_store_dwordx2 v[20:21], v[22:23], off offset:1024
	global_store_dwordx4 v[18:19], v[42:45], off offset:2048
	v_pk_mul_f32 v[22:23], v[26:27], v[0:1] op_sel_hi:[1,0]
	v_pk_mul_f32 v[26:27], v[30:31], v[0:1] op_sel_hi:[1,0]
	v_mov_b32_e32 v32, v1
	v_mov_b32_e32 v33, v1
	v_pk_mul_f32 v[22:23], v[22:23], v[180:181]
	v_pk_mul_f32 v[26:27], v[26:27], v[184:185]
	v_pk_mul_f32 v[24:25], v[24:25], v[182:183]
	v_mul_f32_e32 v0, 0x42000000, v22
	v_mul_f32_e32 v30, 0x42000000, v23
	v_mul_f32_e32 v31, 0x42000000, v24
	v_mul_f32_e32 v41, 0x42000000, v25
	v_mul_f32_e32 v42, 0x42000000, v26
	v_mul_f32_e32 v43, 0x42000000, v27
	v_cvt_pk_bf16_f32 v22, v22, v23
	v_cvt_pk_bf16_f32 v23, v24, v25
	v_med3_f32 v0, v0, s76, v237
	v_med3_f32 v24, v30, s76, v237
	v_med3_f32 v25, v31, s76, v237
	v_med3_f32 v30, v41, s76, v237
	v_med3_f32 v31, v42, s76, v237
	v_med3_f32 v41, v43, s76, v237
	v_cvt_pk_fp8_f32 v32, v0, v24
	v_cvt_pk_fp8_f32 v33, v31, v41
	v_pk_mul_f32 v[28:29], v[28:29], v[186:187]
	v_cvt_pk_bf16_f32 v24, v26, v27
	v_mul_f32_e32 v44, 0x42000000, v28
	v_mul_f32_e32 v45, 0x42000000, v29
	v_med3_f32 v42, v44, s76, v237
	v_med3_f32 v0, v45, s76, v237
	v_cvt_pk_fp8_f32 v32, v25, v30 op_sel:[0,0,1]
	v_cvt_pk_fp8_f32 v33, v42, v0 op_sel:[0,0,1]
	v_cvt_pk_bf16_f32 v25, v28, v29
	global_store_dwordx2 v[20:21], v[32:33], off offset:1536
	global_store_dwordx4 v[18:19], v[22:25], off offset:3072
	s_cbranch_scc0 .LBB0_2271

.LBB0_3598:
	global_load_dwordx4 v[10:13], v[50:51], off offset:-4080
	global_load_dwordx4 v[18:21], v[50:51], off offset:-4096
	global_load_dwordx4 v[2:5], v[50:51], off offset:-2032
	global_load_dwordx4 v[22:25], v[50:51], off offset:-2048
	global_load_dwordx4 v[6:9], v[50:51], off offset:16
	global_load_dwordx4 v[26:29], v[50:51], off
	global_load_dwordx4 v[14:17], v[50:51], off offset:2064
	global_load_dwordx4 v[30:33], v[50:51], off offset:2048
	global_load_dwordx4 v[156:159], v[42:43], off offset:16
	global_load_dwordx4 v[160:163], v[42:43], off
	global_load_dwordx4 v[164:167], v[42:43], off offset:2064
	global_load_dwordx4 v[168:171], v[42:43], off offset:2048
	global_load_dwordx4 v[172:175], v[44:45], off offset:16
	global_load_dwordx4 v[176:179], v[44:45], off
	global_load_dwordx4 v[180:183], v[46:47], off offset:16
	global_load_dwordx4 v[184:187], v[46:47], off
	s_add_i32 s4, s4, s12
	s_cmpk_gt_i32 s4, 0x7ff
	s_waitcnt vmcnt(14)
	v_mul_f32_e32 v0, v19, v19
	v_mul_f32_e32 v188, v21, v21
	v_fmac_f32_e32 v0, v18, v18
	v_fmac_f32_e32 v188, v20, v20
	v_add_f32_e32 v0, v0, v188
	v_mul_f32_e32 v188, v11, v11
	v_fmac_f32_e32 v188, v10, v10
	v_add_f32_e32 v0, v0, v188
	v_mul_f32_e32 v188, v13, v13
	v_fmac_f32_e32 v188, v12, v12
	v_add_f32_e32 v0, v188, v0
	s_waitcnt vmcnt(12)
	v_mul_f32_e32 v188, v23, v23
	v_fmac_f32_e32 v188, v22, v22
	v_add_f32_e32 v0, v188, v0
	v_mul_f32_e32 v188, v25, v25
	v_fmac_f32_e32 v188, v24, v24
	v_add_f32_e32 v0, v188, v0
	v_mul_f32_e32 v188, v3, v3
	v_fmac_f32_e32 v188, v2, v2
	v_add_f32_e32 v0, v188, v0
	v_mul_f32_e32 v188, v5, v5
	v_fmac_f32_e32 v188, v4, v4
	v_add_f32_e32 v0, v188, v0
	s_waitcnt vmcnt(10)
	v_mul_f32_e32 v188, v27, v27
	v_fmac_f32_e32 v188, v26, v26
	v_add_f32_e32 v0, v188, v0
	v_mul_f32_e32 v188, v29, v29
	v_fmac_f32_e32 v188, v28, v28
	v_add_f32_e32 v0, v188, v0
	v_mul_f32_e32 v188, v7, v7
	v_fmac_f32_e32 v188, v6, v6
	v_add_f32_e32 v0, v188, v0
	v_mul_f32_e32 v188, v9, v9
	v_fmac_f32_e32 v188, v8, v8
	v_add_f32_e32 v0, v188, v0
	v_lshl_add_u64 v[50:51], v[50:51], 0, s[86:87]
	s_waitcnt vmcnt(8)
	v_pk_mul_f32 v[34:35], v[32:33], v[32:33]
	v_pk_mul_f32 v[36:37], v[30:31], v[30:31]
	v_mov_b32_e32 v38, v34
	v_mov_b32_e32 v39, v36
	v_mov_b32_e32 v36, v35
	v_pk_add_f32 v[34:35], v[38:39], v[36:37]
	v_pk_mul_f32 v[36:37], v[14:15], v[14:15]
	v_add_f32_e32 v0, v35, v0
	v_add_f32_e32 v0, v34, v0
	v_pk_mul_f32 v[34:35], v[16:17], v[16:17]
	v_mov_b32_e32 v39, v36
	v_mov_b32_e32 v38, v34
	v_mov_b32_e32 v36, v35
	v_pk_add_f32 v[34:35], v[38:39], v[36:37]
	s_nop 0
	v_add_f32_e32 v0, v35, v0
	v_add_f32_e32 v0, v34, v0
	s_nop 1
	v_add_f32_dpp v0, v0, v0 quad_perm:[1,0,3,2] row_mask:0xf bank_mask:0xf
	s_nop 1
	v_add_f32_dpp v0, v0, v0 quad_perm:[2,3,0,1] row_mask:0xf bank_mask:0xf
	s_nop 1
	v_add_f32_dpp v0, v0, v0 row_half_mirror row_mask:0xf bank_mask:0xf
	s_nop 1
	v_add_f32_dpp v0, v0, v0 row_mirror row_mask:0xf bank_mask:0xf
	v_mov_b32_e32 v34, v0
	s_nop 1
	v_permlane16_swap_b32_e32 v0, v34
	v_add_f32_e32 v0, v0, v34
	v_mov_b32_e32 v34, v0
	s_nop 1
	v_permlane32_swap_b32_e32 v0, v34
	v_add_f32_e32 v0, v0, v34
	v_fmamk_f32 v0, v0, 0x3a000000, v220
	v_cmp_gt_f32_e32 vcc, s65, v0
	v_mul_f32_e32 v34, 0x4b800000, v0
	s_nop 0
	v_cndmask_b32_e32 v0, v0, v34, vcc
	v_rsq_f32_e32 v0, v0
	s_nop 0
	v_mul_f32_e32 v34, 0x45800000, v0
	v_cndmask_b32_e32 v0, v0, v34, vcc
	v_pk_mul_f32 v[10:11], v[10:11], v[0:1] op_sel_hi:[1,0]
	v_pk_mul_f32 v[18:19], v[18:19], v[0:1] op_sel_hi:[1,0]
	v_pk_mul_f32 v[2:3], v[2:3], v[0:1] op_sel_hi:[1,0]
	v_pk_mul_f32 v[22:23], v[22:23], v[0:1] op_sel_hi:[1,0]
	v_pk_mul_f32 v[6:7], v[6:7], v[0:1] op_sel_hi:[1,0]
	s_waitcnt vmcnt(7)
	v_pk_mul_f32 v[34:35], v[156:157], v[10:11]
	v_pk_mul_f32 v[10:11], v[20:21], v[0:1] op_sel_hi:[1,0]
	s_waitcnt vmcnt(6)
	v_pk_mul_f32 v[18:19], v[160:161], v[18:19]
	v_pk_mul_f32 v[20:21], v[162:163], v[10:11]
	v_pk_mul_f32 v[10:11], v[12:13], v[0:1] op_sel_hi:[1,0]
	v_cvt_pk_bf16_f32 v12, v34, v35
	v_pk_mul_f32 v[36:37], v[158:159], v[10:11]
	v_cvt_pk_bf16_f32 v10, v18, v19
	v_cvt_pk_bf16_f32 v11, v20, v21
	v_cvt_pk_bf16_f32 v13, v36, v37
	global_store_dwordx4 v[48:49], v[10:13], off
	s_nop 1
	s_waitcnt vmcnt(5)
	v_pk_mul_f32 v[10:11], v[164:165], v[2:3]
	v_pk_mul_f32 v[2:3], v[24:25], v[0:1] op_sel_hi:[1,0]
	s_waitcnt vmcnt(4)
	v_pk_mul_f32 v[18:19], v[168:169], v[22:23]
	v_pk_mul_f32 v[20:21], v[170:171], v[2:3]
	v_pk_mul_f32 v[2:3], v[4:5], v[0:1] op_sel_hi:[1,0]
	v_cvt_pk_bf16_f32 v4, v10, v11
	v_pk_mul_f32 v[12:13], v[166:167], v[2:3]
	v_cvt_pk_bf16_f32 v2, v18, v19
	v_cvt_pk_bf16_f32 v3, v20, v21
	v_cvt_pk_bf16_f32 v5, v12, v13
	global_store_dwordx4 v[48:49], v[2:5], off offset:1024
	s_nop 0
	v_pk_mul_f32 v[18:19], v[26:27], v[0:1] op_sel_hi:[1,0]
	s_waitcnt vmcnt(3)
	v_pk_mul_f32 v[6:7], v[172:173], v[6:7]
	v_pk_mul_f32 v[2:3], v[28:29], v[0:1] op_sel_hi:[1,0]
	s_waitcnt vmcnt(2)
	v_pk_mul_f32 v[10:11], v[176:177], v[18:19]
	v_pk_mul_f32 v[12:13], v[178:179], v[2:3]
	v_pk_mul_f32 v[2:3], v[8:9], v[0:1] op_sel_hi:[1,0]
	s_nop 0
	v_pk_mul_f32 v[8:9], v[174:175], v[2:3]
	v_cvt_pk_bf16_f32 v2, v10, v11
	v_cvt_pk_bf16_f32 v3, v12, v13
	v_cvt_pk_bf16_f32 v4, v6, v7
	v_cvt_pk_bf16_f32 v5, v8, v9
	global_store_dwordx4 v[48:49], v[2:5], off offset:2048
	v_pk_mul_f32 v[10:11], v[30:31], v[0:1] op_sel_hi:[1,0]
	s_waitcnt vmcnt(0)
	v_pk_mul_f32 v[6:7], v[184:185], v[10:11]
	v_pk_mul_f32 v[10:11], v[14:15], v[0:1] op_sel_hi:[1,0]
	s_nop 0
	v_pk_mul_f32 v[10:11], v[180:181], v[10:11]
	v_pk_mul_f32 v[2:3], v[32:33], v[0:1] op_sel_hi:[1,0]
	s_nop 0
	v_pk_mul_f32 v[8:9], v[186:187], v[2:3]
	v_pk_mul_f32 v[2:3], v[16:17], v[0:1] op_sel_hi:[1,0]
	s_nop 0
	v_pk_mul_f32 v[12:13], v[182:183], v[2:3]
	v_cvt_pk_bf16_f32 v2, v6, v7
	v_cvt_pk_bf16_f32 v3, v8, v9
	v_cvt_pk_bf16_f32 v4, v10, v11
	v_cvt_pk_bf16_f32 v5, v12, v13
	global_store_dwordx4 v[48:49], v[2:5], off offset:3072
	v_lshl_add_u64 v[48:49], v[48:49], 0, s[74:75]
	s_cbranch_scc0 .LBB0_3598

.LBB0_7076:
	v_lshl_add_u64 v[0:1], s[8:9], 0, v[54:55]
	v_add_co_u32_e32 v8, vcc, s6, v0
	v_lshl_add_u64 v[54:55], v[54:55], 0, s[74:75]
	s_nop 0
	v_addc_co_u32_e32 v9, vcc, 0, v1, vcc
	s_add_u32 s10, s8, s3
	s_addc_u32 s11, s9, s4
	s_add_i32 s2, s2, s16
	v_readfirstlane_b32 s12, v188
	v_readfirstlane_b32 s14, v190
	s_lshl_b32 s12, s12, 2
	s_lshl_b32 s14, s14, 2
	s_add_i32 s12, s5, s12
	s_add_i32 s14, s5, s14
	v_mov_b32_e32 v0, s12
	v_readfirstlane_b32 s13, v189
	v_mov_b32_e32 v1, s14
	ds_read_b32 v10, v0
	ds_read_b32 v11, v1
	v_readfirstlane_b32 s15, v191
	s_add_u32 s98, s0, s80
	s_addc_u32 s99, s1, s81
	s_add_u32 s98, s98, s8
	s_addc_u32 s99, s99, s9
	global_load_dwordx4 v[188:191], v44, s[98:99]
	global_load_dwordx4 v[66:69], v[8:9], off
	global_load_dwordx4 v[82:85], v[8:9], off offset:1024
	global_load_dwordx4 v[86:89], v[8:9], off offset:2048
	global_load_dwordx4 v[32:35], v[8:9], off offset:3072
	global_load_dwordx2 v[58:59], v45, s[10:11]
	s_waitcnt lgkmcnt(1)
	v_readfirstlane_b32 s10, v10
	s_waitcnt lgkmcnt(0)
	v_readfirstlane_b32 s11, v11
	s_lshl_b32 s11, s11, 8
	s_lshl_b32 s10, s10, 8
	s_add_i32 s12, s11, s15
	s_add_i32 s10, s10, s13
	s_ashr_i32 s13, s12, 31
	s_ashr_i32 s11, s10, 31
	s_lshl_b64 s[12:13], s[12:13], 12
	s_lshl_b64 s[10:11], s[10:11], 12
	v_lshl_add_u64 v[62:63], v[52:53], 0, s[12:13]
	v_lshl_add_u64 v[60:61], v[52:53], 0, s[10:11]
	global_load_dwordx4 v[36:39], v[62:63], off
	global_load_dwordx4 v[40:43], v[60:61], off
	global_load_dwordx4 v[24:27], v[62:63], off offset:1024
	global_load_dwordx4 v[28:31], v[60:61], off offset:1024
	global_load_dwordx4 v[16:19], v[62:63], off offset:2048
	global_load_dwordx4 v[20:23], v[60:61], off offset:2048
	global_load_dwordx4 v[8:11], v[60:61], off offset:3072
	global_load_dwordx4 v[12:15], v[62:63], off offset:3072
	s_add_u32 s0, s0, s80
	s_addc_u32 s1, s1, s81
	s_add_u32 s3, s3, s84
	s_addc_u32 s4, s4, s85
	s_cmpk_lt_i32 s2, 0x4000
	s_waitcnt vmcnt(12)
	v_lshlrev_b32_e32 v64, 16, v66
	v_and_b32_e32 v65, 0xffff0000, v66
	v_lshlrev_b32_e32 v66, 16, v67
	v_and_b32_e32 v67, 0xffff0000, v67
	v_lshlrev_b32_e32 v60, 16, v68
	v_and_b32_e32 v61, 0xffff0000, v68
	v_lshlrev_b32_e32 v62, 16, v69
	v_and_b32_e32 v63, 0xffff0000, v69
	s_waitcnt vmcnt(9)
	v_lshlrev_b32_e32 v94, 16, v32
	v_and_b32_e32 v95, 0xffff0000, v32
	v_lshlrev_b32_e32 v32, 16, v33
	v_and_b32_e32 v33, 0xffff0000, v33
	v_lshlrev_b32_e32 v72, 16, v82
	s_waitcnt vmcnt(7)
	v_and_b32_e32 v99, 0xffff0000, v38
	s_waitcnt vmcnt(6)
	v_and_b32_e32 v97, 0xffff0000, v42
	v_lshlrev_b32_e32 v98, 16, v42
	v_lshlrev_b32_e32 v42, 16, v36
	v_lshlrev_b32_e32 v102, 16, v40
	v_and_b32_e32 v103, 0xffff0000, v36
	v_lshlrev_b32_e32 v104, 16, v37
	v_lshlrev_b32_e32 v36, 16, v41
	v_and_b32_e32 v37, 0xffff0000, v37
	v_lshlrev_b32_e32 v96, 16, v38
	v_and_b32_e32 v101, 0xffff0000, v43
	v_lshlrev_b32_e32 v38, 16, v43
	v_and_b32_e32 v43, 0xffff0000, v40
	v_and_b32_e32 v105, 0xffff0000, v41
	s_waitcnt vmcnt(5)
	v_lshlrev_b32_e32 v40, 16, v26
	s_waitcnt vmcnt(4)
	v_and_b32_e32 v41, 0xffff0000, v30
	v_lshlrev_b32_e32 v106, 16, v30
	v_and_b32_e32 v107, 0xffff0000, v26
	v_and_b32_e32 v109, 0xffff0000, v31
	v_lshlrev_b32_e32 v26, 16, v31
	v_lshlrev_b32_e32 v30, 16, v24
	v_and_b32_e32 v31, 0xffff0000, v28
	v_lshlrev_b32_e32 v110, 16, v28
	v_and_b32_e32 v111, 0xffff0000, v24
	v_and_b32_e32 v113, 0xffff0000, v29
	v_lshlrev_b32_e32 v24, 16, v29
	s_waitcnt vmcnt(3)
	v_lshlrev_b32_e32 v28, 16, v18
	s_waitcnt vmcnt(2)
	v_and_b32_e32 v29, 0xffff0000, v22
	v_lshlrev_b32_e32 v114, 16, v22
	v_and_b32_e32 v115, 0xffff0000, v18
	v_and_b32_e32 v117, 0xffff0000, v23
	v_lshlrev_b32_e32 v18, 16, v23
	v_lshlrev_b32_e32 v22, 16, v16
	v_and_b32_e32 v23, 0xffff0000, v20
	v_lshlrev_b32_e32 v118, 16, v20
	v_and_b32_e32 v119, 0xffff0000, v16
	v_and_b32_e32 v121, 0xffff0000, v21
	v_lshlrev_b32_e32 v16, 16, v21
	s_waitcnt vmcnt(0)
	v_lshlrev_b32_e32 v20, 16, v14
	v_and_b32_e32 v21, 0xffff0000, v10
	v_lshlrev_b32_e32 v122, 16, v10
	v_and_b32_e32 v123, 0xffff0000, v14
	v_lshlrev_b32_e32 v124, 16, v15
	v_and_b32_e32 v125, 0xffff0000, v11
	v_lshlrev_b32_e32 v10, 16, v11
	v_and_b32_e32 v11, 0xffff0000, v15
	v_lshlrev_b32_e32 v14, 16, v12
	v_and_b32_e32 v15, 0xffff0000, v8
	v_lshlrev_b32_e32 v126, 16, v8
	v_and_b32_e32 v127, 0xffff0000, v12
	v_lshlrev_b32_e32 v128, 16, v13
	v_and_b32_e32 v129, 0xffff0000, v9
	v_lshlrev_b32_e32 v8, 16, v9
	v_and_b32_e32 v9, 0xffff0000, v13
	v_pk_mul_f32 v[12:13], v[58:59], v[98:99]
	v_pk_mul_f32 v[98:99], v[58:59], v[102:103]
	v_pk_mul_f32 v[36:37], v[58:59], v[36:37]
	v_lshlrev_b32_e32 v100, 16, v39
	v_and_b32_e32 v39, 0xffff0000, v39
	v_lshlrev_b32_e32 v108, 16, v27
	v_and_b32_e32 v27, 0xffff0000, v27
	v_lshlrev_b32_e32 v112, 16, v25
	v_and_b32_e32 v25, 0xffff0000, v25
	v_lshlrev_b32_e32 v116, 16, v19
	v_and_b32_e32 v19, 0xffff0000, v19
	v_lshlrev_b32_e32 v120, 16, v17
	v_and_b32_e32 v17, 0xffff0000, v17
	v_pk_fma_f32 v[42:43], v[58:59], v[42:43], v[98:99] op_sel:[1,0,0] op_sel_hi:[0,1,1]
	v_pk_fma_f32 v[36:37], v[58:59], v[104:105], v[36:37] op_sel:[1,0,0] op_sel_hi:[0,1,1]
	v_pk_mul_f32 v[38:39], v[58:59], v[38:39]
	v_pk_mul_f32 v[102:103], v[58:59], v[106:107]
	v_pk_mul_f32 v[26:27], v[58:59], v[26:27]
	v_pk_mul_f32 v[106:107], v[58:59], v[110:111]
	v_pk_mul_f32 v[24:25], v[58:59], v[24:25]
	v_pk_mul_f32 v[110:111], v[58:59], v[114:115]
	v_pk_mul_f32 v[18:19], v[58:59], v[18:19]
	v_pk_mul_f32 v[114:115], v[58:59], v[118:119]
	v_pk_mul_f32 v[16:17], v[58:59], v[16:17]
	v_pk_mul_f32 v[118:119], v[58:59], v[122:123]
	v_pk_mul_f32 v[10:11], v[58:59], v[10:11]
	v_pk_mul_f32 v[122:123], v[58:59], v[126:127]
	v_pk_mul_f32 v[8:9], v[58:59], v[8:9]
	v_pk_fma_f32 v[12:13], v[58:59], v[96:97], v[12:13] op_sel:[1,0,0] op_sel_hi:[0,1,1]
	v_pk_add_f32 v[42:43], v[42:43], v[64:65]
	v_pk_add_f32 v[36:37], v[36:37], v[66:67]
	v_pk_fma_f32 v[38:39], v[58:59], v[100:101], v[38:39] op_sel:[1,0,0] op_sel_hi:[0,1,1]
	v_pk_fma_f32 v[40:41], v[58:59], v[40:41], v[102:103] op_sel:[1,0,0] op_sel_hi:[0,1,1]
	v_pk_fma_f32 v[26:27], v[58:59], v[108:109], v[26:27] op_sel:[1,0,0] op_sel_hi:[0,1,1]
	v_pk_fma_f32 v[30:31], v[58:59], v[30:31], v[106:107] op_sel:[1,0,0] op_sel_hi:[0,1,1]
	v_pk_fma_f32 v[24:25], v[58:59], v[112:113], v[24:25] op_sel:[1,0,0] op_sel_hi:[0,1,1]
	v_pk_fma_f32 v[28:29], v[58:59], v[28:29], v[110:111] op_sel:[1,0,0] op_sel_hi:[0,1,1]
	v_pk_fma_f32 v[18:19], v[58:59], v[116:117], v[18:19] op_sel:[1,0,0] op_sel_hi:[0,1,1]
	v_pk_fma_f32 v[22:23], v[58:59], v[22:23], v[114:115] op_sel:[1,0,0] op_sel_hi:[0,1,1]
	v_pk_fma_f32 v[16:17], v[58:59], v[120:121], v[16:17] op_sel:[1,0,0] op_sel_hi:[0,1,1]
	v_pk_fma_f32 v[20:21], v[58:59], v[20:21], v[118:119] op_sel:[1,0,0] op_sel_hi:[0,1,1]
	v_pk_fma_f32 v[10:11], v[58:59], v[124:125], v[10:11] op_sel:[1,0,0] op_sel_hi:[0,1,1]
	v_pk_fma_f32 v[14:15], v[58:59], v[14:15], v[122:123] op_sel:[1,0,0] op_sel_hi:[0,1,1]
	v_pk_fma_f32 v[8:9], v[58:59], v[128:129], v[8:9] op_sel:[1,0,0] op_sel_hi:[0,1,1]
	v_pk_add_f32 v[12:13], v[12:13], v[60:61]
	v_pk_mul_f32 v[58:59], v[42:43], v[42:43]
	v_pk_mul_f32 v[60:61], v[36:37], v[36:37]
	v_and_b32_e32 v73, 0xffff0000, v82
	v_lshlrev_b32_e32 v92, 16, v34
	v_and_b32_e32 v93, 0xffff0000, v34
	v_lshlrev_b32_e32 v34, 16, v35
	v_and_b32_e32 v35, 0xffff0000, v35
	v_pk_add_f32 v[38:39], v[38:39], v[62:63]
	v_pk_add_f32 v[8:9], v[8:9], v[32:33]
	v_pk_mul_f32 v[32:33], v[12:13], v[12:13]
	v_add_f32_e32 v60, v60, v61
	v_add_f32_e32 v58, v58, v59
	v_lshlrev_b32_e32 v82, 16, v83
	v_and_b32_e32 v83, 0xffff0000, v83
	v_pk_add_f32 v[30:31], v[30:31], v[72:73]
	v_pk_add_f32 v[10:11], v[10:11], v[34:35]
	v_pk_mul_f32 v[34:35], v[38:39], v[38:39]
	v_add_f32_e32 v59, v32, v33
	v_add_f32_e32 v58, v58, v60
	v_lshlrev_b32_e32 v68, 16, v84
	v_and_b32_e32 v69, 0xffff0000, v84
	v_pk_add_f32 v[24:25], v[24:25], v[82:83]
	v_pk_mul_f32 v[66:67], v[30:31], v[30:31]
	v_add_f32_e32 v81, v34, v35
	v_add_f32_e32 v58, v59, v58
	v_lshlrev_b32_e32 v70, 16, v85
	v_and_b32_e32 v71, 0xffff0000, v85
	v_pk_add_f32 v[40:41], v[40:41], v[68:69]
	v_pk_mul_f32 v[68:69], v[24:25], v[24:25]
	v_add_f32_e32 v61, v66, v67
	v_add_f32_e32 v58, v81, v58
	v_lshlrev_b32_e32 v90, 16, v86
	v_and_b32_e32 v91, 0xffff0000, v86
	v_pk_add_f32 v[26:27], v[26:27], v[70:71]
	v_pk_mul_f32 v[62:63], v[40:41], v[40:41]
	v_add_f32_e32 v66, v68, v69
	v_add_f32_e32 v58, v58, v61
	v_lshlrev_b32_e32 v86, 16, v87
	v_and_b32_e32 v87, 0xffff0000, v87
	v_pk_add_f32 v[22:23], v[22:23], v[90:91]
	v_pk_mul_f32 v[64:65], v[26:27], v[26:27]
	v_add_f32_e32 v62, v62, v63
	v_add_f32_e32 v58, v66, v58
	v_lshlrev_b32_e32 v84, 16, v88
	v_and_b32_e32 v85, 0xffff0000, v88
	v_pk_add_f32 v[16:17], v[16:17], v[86:87]
	v_pk_mul_f32 v[82:83], v[22:23], v[22:23]
	v_add_f32_e32 v63, v64, v65
	v_add_f32_e32 v58, v62, v58
	v_lshlrev_b32_e32 v88, 16, v89
	v_and_b32_e32 v89, 0xffff0000, v89
	v_pk_add_f32 v[28:29], v[28:29], v[84:85]
	v_pk_mul_f32 v[84:85], v[16:17], v[16:17]
	v_add_f32_e32 v64, v82, v83
	v_add_f32_e32 v58, v63, v58
	v_pk_add_f32 v[18:19], v[18:19], v[88:89]
	v_pk_add_f32 v[14:15], v[14:15], v[94:95]
	v_pk_mul_f32 v[70:71], v[28:29], v[28:29]
	v_add_f32_e32 v65, v84, v85
	v_add_f32_e32 v58, v64, v58
	v_pk_add_f32 v[20:21], v[20:21], v[92:93]
	v_pk_mul_f32 v[72:73], v[18:19], v[18:19]
	v_mov_b32_e32 v92, v9
	v_mov_b32_e32 v93, v15
	v_add_f32_e32 v67, v70, v71
	v_add_f32_e32 v58, v65, v58
	v_mov_b32_e32 v90, v8
	v_mov_b32_e32 v91, v14
	v_pk_mul_f32 v[92:93], v[92:93], v[92:93]
	v_add_f32_e32 v68, v72, v73
	v_add_f32_e32 v58, v67, v58
	v_mov_b32_e32 v88, v11
	v_mov_b32_e32 v89, v21
	v_pk_fma_f32 v[34:35], v[90:91], v[90:91], v[92:93]
	v_add_f32_e32 v58, v68, v58
	v_mov_b32_e32 v86, v10
	v_mov_b32_e32 v87, v20
	v_pk_mul_f32 v[88:89], v[88:89], v[88:89]
	v_add_f32_e32 v35, v35, v58
	v_pk_fma_f32 v[32:33], v[86:87], v[86:87], v[88:89]
	v_add_f32_e32 v34, v34, v35
	v_add_f32_e32 v33, v33, v34
	v_add_f32_e32 v32, v32, v33
	s_nop 1
	v_add_f32_dpp v32, v32, v32 quad_perm:[1,0,3,2] row_mask:0xf bank_mask:0xf
	s_nop 1
	v_add_f32_dpp v32, v32, v32 quad_perm:[2,3,0,1] row_mask:0xf bank_mask:0xf
	s_nop 1
	v_add_f32_dpp v32, v32, v32 row_half_mirror row_mask:0xf bank_mask:0xf
	s_nop 1
	v_add_f32_dpp v32, v32, v32 row_mirror row_mask:0xf bank_mask:0xf
	v_mov_b32_e32 v33, v32
	s_nop 1
	v_permlane16_swap_b32_e32 v32, v33
	v_add_f32_e32 v32, v32, v33
	v_mov_b32_e32 v33, v32
	s_nop 1
	v_permlane32_swap_b32_e32 v32, v33
	v_add_f32_e32 v32, v32, v33
	v_fmamk_f32 v32, v32, 0x3a000000, v80
	v_mul_f32_e32 v33, 0x4b800000, v32
	v_cmp_gt_f32_e32 vcc, s7, v32
	s_nop 1
	v_cndmask_b32_e32 v32, v32, v33, vcc
	v_rsq_f32_e32 v32, v32
	s_nop 0
	v_mul_f32_e32 v33, 0x45800000, v32
	v_cndmask_b32_e32 v32, v32, v33, vcc
	v_pk_mul_f32 v[34:35], v[42:43], v[32:33] op_sel_hi:[1,0]
	v_pk_mul_f32 v[36:37], v[36:37], v[32:33] op_sel_hi:[1,0]
	v_pk_mul_f32 v[12:13], v[12:13], v[32:33] op_sel_hi:[1,0]
	v_pk_mul_f32 v[38:39], v[38:39], v[32:33] op_sel_hi:[1,0]
	v_pk_mul_f32 v[6:7], v[162:163], v[36:37]
	v_pk_mul_f32 v[4:5], v[160:161], v[34:35]
	v_pk_mul_f32 v[2:3], v[158:159], v[38:39]
	v_pk_mul_f32 v[0:1], v[156:157], v[12:13]
	global_store_dwordx4 v[56:57], v[4:7], off offset:-4096 nt
	global_store_dwordx4 v[56:57], v[0:3], off offset:-4080 nt
	v_pk_mul_f32 v[12:13], v[24:25], v[32:33] op_sel_hi:[1,0]
	v_pk_mul_f32 v[24:25], v[30:31], v[32:33] op_sel_hi:[1,0]
	v_pk_mul_f32 v[26:27], v[26:27], v[32:33] op_sel_hi:[1,0]
	v_pk_mul_f32 v[30:31], v[40:41], v[32:33] op_sel_hi:[1,0]
	v_pk_mul_f32 v[18:19], v[18:19], v[32:33] op_sel_hi:[1,0]
	v_pk_mul_f32 v[8:9], v[8:9], v[32:33] op_sel_hi:[1,0]
	v_pk_mul_f32 v[10:11], v[10:11], v[32:33] op_sel_hi:[1,0]
	v_pk_mul_f32 v[0:1], v[164:165], v[24:25]
	v_pk_mul_f32 v[2:3], v[166:167], v[12:13]
	v_pk_mul_f32 v[4:5], v[168:169], v[30:31]
	v_pk_mul_f32 v[6:7], v[170:171], v[26:27]
	global_store_dwordx4 v[56:57], v[0:3], off offset:-2048 nt
	global_store_dwordx4 v[56:57], v[4:7], off offset:-2032 nt
	v_pk_mul_f32 v[12:13], v[16:17], v[32:33] op_sel_hi:[1,0]
	v_pk_mul_f32 v[16:17], v[22:23], v[32:33] op_sel_hi:[1,0]
	v_pk_mul_f32 v[22:23], v[28:29], v[32:33] op_sel_hi:[1,0]
	v_pk_mul_f32 v[0:1], v[172:173], v[16:17]
	v_pk_mul_f32 v[2:3], v[174:175], v[12:13]
	v_pk_mul_f32 v[4:5], v[176:177], v[22:23]
	v_pk_mul_f32 v[6:7], v[178:179], v[18:19]
	global_store_dwordx4 v[56:57], v[0:3], off nt
	global_store_dwordx4 v[56:57], v[4:7], off offset:16 nt
	v_pk_mul_f32 v[12:13], v[14:15], v[32:33] op_sel_hi:[1,0]
	v_pk_mul_f32 v[14:15], v[20:21], v[32:33] op_sel_hi:[1,0]
	v_pk_mul_f32 v[0:1], v[180:181], v[12:13]
	v_pk_mul_f32 v[2:3], v[182:183], v[8:9]
	v_pk_mul_f32 v[4:5], v[184:185], v[14:15]
	v_pk_mul_f32 v[6:7], v[186:187], v[10:11]
	global_store_dwordx4 v[56:57], v[0:3], off offset:2048 nt
	global_store_dwordx4 v[56:57], v[4:7], off offset:2064 nt
	v_lshl_add_u64 v[56:57], v[56:57], 0, s[86:87]
	s_cbranch_scc1 .LBB0_7076
